# MoE K-loops: pipelined fragment reads + f32->bf16 conversion/ds_write of staged weights interleaved into MFMA block 4 with per-load counted vmcnt waits
# speedup vs baseline: 1.0130x; 1.0048x over previous
.LBB0_726:
	s_cmp_lg_u64 s[2:3], 0
	s_cbranch_scc1 .Lswp_guE_half
	ds_read_b64_tr_b16 v[162:163], v190 offset:0
	ds_read_b64_tr_b16 v[164:165], v191 offset:0
	ds_read_b64_tr_b16 v[166:167], v190 offset:8192
	ds_read_b64_tr_b16 v[168:169], v191 offset:8192
	ds_read_b64_tr_b16 v[170:171], v192 offset:0
	ds_read_b64_tr_b16 v[172:173], v193 offset:0
	ds_read_b64_tr_b16 v[174:175], v192 offset:8192
	ds_read_b64_tr_b16 v[176:177], v193 offset:8192
	ds_read_b128 v[214:217], v207
	ds_read_b128 v[224:227], v207 offset:2048
	ds_read_b128 v[232:235], v207 offset:4096
	ds_read_b128 v[240:243], v207 offset:6144
	ds_read_b128 v[218:221], v207 offset:1024
	ds_read_b128 v[228:231], v207 offset:3072
	ds_read_b128 v[236:239], v207 offset:5120
	ds_read_b128 v[244:247], v207 offset:7168
	s_setprio 1
	s_waitcnt lgkmcnt(7)
	v_mfma_f32_16x16x32_bf16 v[158:161], v[162:165], v[214:217], v[158:161]
	v_mfma_f32_16x16x32_bf16 v[154:157], v[170:173], v[214:217], v[154:157]
	ds_read_b128 v[214:217], v207 offset:16384
	s_waitcnt lgkmcnt(7)
	v_mfma_f32_16x16x32_bf16 v[146:149], v[162:165], v[224:227], v[146:149]
	v_mfma_f32_16x16x32_bf16 v[138:141], v[170:173], v[224:227], v[138:141]
	ds_read_b128 v[224:227], v207 offset:18432
	s_waitcnt lgkmcnt(7)
	v_mfma_f32_16x16x32_bf16 v[130:133], v[162:165], v[232:235], v[130:133]
	v_mfma_f32_16x16x32_bf16 v[122:125], v[170:173], v[232:235], v[122:125]
	ds_read_b128 v[232:235], v207 offset:20480
	s_waitcnt lgkmcnt(7)
	v_mfma_f32_16x16x32_bf16 v[114:117], v[162:165], v[240:243], v[114:117]
	v_mfma_f32_16x16x32_bf16 v[106:109], v[170:173], v[240:243], v[106:109]
	ds_read_b128 v[240:243], v207 offset:22528
	s_waitcnt lgkmcnt(7)
	v_mfma_f32_16x16x32_bf16 v[158:161], v[166:169], v[218:221], v[158:161]
	v_mfma_f32_16x16x32_bf16 v[154:157], v[174:177], v[218:221], v[154:157]
	ds_read_b128 v[218:221], v207 offset:17408
	s_waitcnt lgkmcnt(7)
	v_mfma_f32_16x16x32_bf16 v[146:149], v[166:169], v[228:231], v[146:149]
	v_mfma_f32_16x16x32_bf16 v[138:141], v[174:177], v[228:231], v[138:141]
	ds_read_b128 v[228:231], v207 offset:19456
	s_waitcnt lgkmcnt(7)
	v_mfma_f32_16x16x32_bf16 v[130:133], v[166:169], v[236:239], v[130:133]
	v_mfma_f32_16x16x32_bf16 v[122:125], v[174:177], v[236:239], v[122:125]
	ds_read_b128 v[236:239], v207 offset:21504
	s_waitcnt lgkmcnt(7)
	v_mfma_f32_16x16x32_bf16 v[114:117], v[166:169], v[244:247], v[114:117]
	v_mfma_f32_16x16x32_bf16 v[106:109], v[174:177], v[244:247], v[106:109]
	ds_read_b128 v[244:247], v207 offset:23552
	s_waitcnt lgkmcnt(7)
	v_mfma_f32_16x16x32_bf16 v[94:97], v[162:165], v[214:217], v[94:97]
	v_mfma_f32_16x16x32_bf16 v[86:89], v[170:173], v[214:217], v[86:89]
	ds_read_b128 v[214:217], v207
	s_waitcnt lgkmcnt(7)
	v_mfma_f32_16x16x32_bf16 v[78:81], v[162:165], v[224:227], v[78:81]
	v_mfma_f32_16x16x32_bf16 v[70:73], v[170:173], v[224:227], v[70:73]
	ds_read_b128 v[224:227], v207 offset:2048
	s_waitcnt lgkmcnt(7)
	v_mfma_f32_16x16x32_bf16 v[62:65], v[162:165], v[232:235], v[62:65]
	v_mfma_f32_16x16x32_bf16 v[54:57], v[170:173], v[232:235], v[54:57]
	ds_read_b128 v[232:235], v207 offset:4096
	s_waitcnt lgkmcnt(7)
	v_mfma_f32_16x16x32_bf16 v[46:49], v[162:165], v[240:243], v[46:49]
	v_mfma_f32_16x16x32_bf16 v[38:41], v[170:173], v[240:243], v[38:41]
	ds_read_b128 v[240:243], v207 offset:6144
	ds_read_b64_tr_b16 v[162:163], v190 offset:16384
	ds_read_b64_tr_b16 v[164:165], v191 offset:16384
	ds_read_b64_tr_b16 v[170:171], v192 offset:16384
	ds_read_b64_tr_b16 v[172:173], v193 offset:16384
	s_waitcnt lgkmcnt(11)
	v_mfma_f32_16x16x32_bf16 v[94:97], v[166:169], v[218:221], v[94:97]
	v_mfma_f32_16x16x32_bf16 v[86:89], v[174:177], v[218:221], v[86:89]
	ds_read_b128 v[218:221], v207 offset:1024
	s_waitcnt lgkmcnt(11)
	v_mfma_f32_16x16x32_bf16 v[78:81], v[166:169], v[228:231], v[78:81]
	v_mfma_f32_16x16x32_bf16 v[70:73], v[174:177], v[228:231], v[70:73]
	ds_read_b128 v[228:231], v207 offset:3072
	s_waitcnt lgkmcnt(11)
	v_mfma_f32_16x16x32_bf16 v[62:65], v[166:169], v[236:239], v[62:65]
	v_mfma_f32_16x16x32_bf16 v[54:57], v[174:177], v[236:239], v[54:57]
	ds_read_b128 v[236:239], v207 offset:5120
	s_waitcnt lgkmcnt(11)
	v_mfma_f32_16x16x32_bf16 v[46:49], v[166:169], v[244:247], v[46:49]
	v_mfma_f32_16x16x32_bf16 v[38:41], v[174:177], v[244:247], v[38:41]
	ds_read_b128 v[244:247], v207 offset:7168
	ds_read_b64_tr_b16 v[166:167], v190 offset:24576
	ds_read_b64_tr_b16 v[168:169], v191 offset:24576
	ds_read_b64_tr_b16 v[174:175], v192 offset:24576
	ds_read_b64_tr_b16 v[176:177], v193 offset:24576
	s_waitcnt lgkmcnt(8)
	v_mfma_f32_16x16x32_bf16 v[150:153], v[162:165], v[214:217], v[150:153]
	v_mfma_f32_16x16x32_bf16 v[142:145], v[170:173], v[214:217], v[142:145]
	ds_read_b128 v[214:217], v207 offset:16384
	v_mfma_f32_16x16x32_bf16 v[134:137], v[162:165], v[224:227], v[134:137]
	v_mfma_f32_16x16x32_bf16 v[126:129], v[170:173], v[224:227], v[126:129]
	ds_read_b128 v[224:227], v207 offset:18432
	v_mfma_f32_16x16x32_bf16 v[118:121], v[162:165], v[232:235], v[118:121]
	v_mfma_f32_16x16x32_bf16 v[110:113], v[170:173], v[232:235], v[110:113]
	ds_read_b128 v[232:235], v207 offset:20480
	v_mfma_f32_16x16x32_bf16 v[102:105], v[162:165], v[240:243], v[102:105]
	v_mfma_f32_16x16x32_bf16 v[98:101], v[170:173], v[240:243], v[98:101]
	ds_read_b128 v[240:243], v207 offset:22528
	s_waitcnt lgkmcnt(4)
	v_mfma_f32_16x16x32_bf16 v[150:153], v[166:169], v[218:221], v[150:153]
	v_mfma_f32_16x16x32_bf16 v[142:145], v[174:177], v[218:221], v[142:145]
	ds_read_b128 v[218:221], v207 offset:17408
	v_mfma_f32_16x16x32_bf16 v[134:137], v[166:169], v[228:231], v[134:137]
	v_mfma_f32_16x16x32_bf16 v[126:129], v[174:177], v[228:231], v[126:129]
	ds_read_b128 v[228:231], v207 offset:19456
	v_mfma_f32_16x16x32_bf16 v[118:121], v[166:169], v[236:239], v[118:121]
	v_mfma_f32_16x16x32_bf16 v[110:113], v[174:177], v[236:239], v[110:113]
	ds_read_b128 v[236:239], v207 offset:21504
	v_mfma_f32_16x16x32_bf16 v[102:105], v[166:169], v[244:247], v[102:105]
	v_mfma_f32_16x16x32_bf16 v[98:101], v[174:177], v[244:247], v[98:101]
	ds_read_b128 v[244:247], v207 offset:23552
	s_waitcnt lgkmcnt(7)
	v_mfma_f32_16x16x32_bf16 v[90:93], v[162:165], v[214:217], v[90:93]
	v_mfma_f32_16x16x32_bf16 v[82:85], v[170:173], v[214:217], v[82:85]
	s_waitcnt vmcnt(11)
	v_cvt_pk_bf16_f32 v2, v2, v3
	v_cvt_pk_bf16_f32 v3, v4, v5
	ds_write_b64 v199, v[2:3]
	s_waitcnt lgkmcnt(7)
	v_mfma_f32_16x16x32_bf16 v[74:77], v[162:165], v[224:227], v[74:77]
	v_mfma_f32_16x16x32_bf16 v[66:69], v[170:173], v[224:227], v[66:69]
	s_waitcnt vmcnt(10)
	v_cvt_pk_bf16_f32 v2, v6, v7
	v_cvt_pk_bf16_f32 v3, v8, v9
	ds_write_b64 v200, v[2:3]
	s_waitcnt lgkmcnt(7)
	v_mfma_f32_16x16x32_bf16 v[58:61], v[162:165], v[232:235], v[58:61]
	v_mfma_f32_16x16x32_bf16 v[50:53], v[170:173], v[232:235], v[50:53]
	s_waitcnt vmcnt(9)
	v_cvt_pk_bf16_f32 v2, v10, v11
	v_cvt_pk_bf16_f32 v3, v12, v13
	ds_write_b64 v201, v[2:3]
	s_waitcnt lgkmcnt(7)
	v_mfma_f32_16x16x32_bf16 v[42:45], v[162:165], v[240:243], v[42:45]
	v_mfma_f32_16x16x32_bf16 v[30:33], v[170:173], v[240:243], v[30:33]
	s_waitcnt vmcnt(8)
	v_cvt_pk_bf16_f32 v2, v14, v15
	v_cvt_pk_bf16_f32 v3, v16, v17
	ds_write_b64 v202, v[2:3]
	s_waitcnt lgkmcnt(7)
	v_mfma_f32_16x16x32_bf16 v[90:93], v[166:169], v[218:221], v[90:93]
	v_mfma_f32_16x16x32_bf16 v[82:85], v[174:177], v[218:221], v[82:85]
	s_waitcnt vmcnt(7)
	v_cvt_pk_bf16_f32 v2, v18, v19
	v_cvt_pk_bf16_f32 v3, v20, v21
	ds_write_b64 v203, v[2:3]
	s_waitcnt lgkmcnt(7)
	v_mfma_f32_16x16x32_bf16 v[74:77], v[166:169], v[228:231], v[74:77]
	v_mfma_f32_16x16x32_bf16 v[66:69], v[174:177], v[228:231], v[66:69]
	s_waitcnt vmcnt(6)
	v_cvt_pk_bf16_f32 v2, v22, v23
	v_cvt_pk_bf16_f32 v3, v24, v25
	ds_write_b64 v204, v[2:3]
	s_waitcnt lgkmcnt(7)
	v_mfma_f32_16x16x32_bf16 v[58:61], v[166:169], v[236:239], v[58:61]
	v_mfma_f32_16x16x32_bf16 v[50:53], v[174:177], v[236:239], v[50:53]
	s_waitcnt vmcnt(5)
	v_cvt_pk_bf16_f32 v2, v26, v27
	v_cvt_pk_bf16_f32 v3, v28, v29
	ds_write_b64 v205, v[2:3]
	s_waitcnt lgkmcnt(7)
	v_mfma_f32_16x16x32_bf16 v[42:45], v[166:169], v[244:247], v[42:45]
	v_mfma_f32_16x16x32_bf16 v[30:33], v[174:177], v[244:247], v[30:33]
	s_waitcnt vmcnt(4)
	v_cvt_pk_bf16_f32 v2, v34, v35
	v_cvt_pk_bf16_f32 v3, v36, v37
	ds_write_b64 v206, v[2:3]
	s_setprio 0

.Lswp_guE_tail:
	s_ashr_i32 s39, s38, 31
	s_lshl_b64 s[40:41], s[38:39], 18
	s_add_u32 s68, s67, s40
	s_addc_u32 s69, s66, s41
	s_add_u32 s40, s35, s40
	s_addc_u32 s41, s34, s41
	s_add_u32 s70, s68, 0x2000
	s_addc_u32 s71, s69, 0
	global_load_dwordx4 v[34:37], v189, s[68:69]
	s_add_u32 s72, s40, 0x2000
	global_load_dwordx4 v[22:25], v189, s[40:41]
	s_addc_u32 s73, s41, 0
	global_load_dwordx4 v[26:29], v189, s[70:71]
	s_add_u32 s70, s68, 0x4000
	s_addc_u32 s71, s69, 0
	global_load_dwordx4 v[14:17], v189, s[72:73]
	s_add_u32 s72, s40, 0x4000
	s_addc_u32 s73, s41, 0
	s_add_u32 s68, s68, 0x6000
	global_load_dwordx4 v[18:21], v189, s[70:71]
	s_addc_u32 s69, s69, 0
	global_load_dwordx4 v[6:9], v189, s[72:73]
	s_add_u32 s40, s40, 0x6000
	s_addc_u32 s41, s41, 0
	global_load_dwordx4 v[10:13], v189, s[68:69]
	global_load_dwordx4 v[2:5], v189, s[40:41]
	s_lshl_b64 s[40:41], s[38:39], 7
	s_add_u32 s40, s8, s40
	s_mov_b32 m0, s51
	s_waitcnt vmcnt(8)
	s_waitcnt lgkmcnt(0)
	s_barrier
	s_addc_u32 s41, s9, s41
	v_cndmask_b32_e64 v164, v178, v209, s[4:5]
	v_cndmask_b32_e64 v163, v180, v210, s[4:5]
	global_load_lds_dwordx4 v164, s[40:41]
	s_mov_b32 m0, s60
	v_cndmask_b32_e64 v162, v213, v208, s[4:5]
	global_load_lds_dwordx4 v163, s[40:41]
	v_cmp_ne_u32_e32 vcc, 0, v162
	s_mov_b64 s[96:97], vcc
	s_cbranch_vccnz .LBB0_732
	v_cndmask_b32_e64 v163, v182, v211, s[4:5]
	s_add_i32 m0, s51, 0x4000
	v_cndmask_b32_e64 v162, v184, v212, s[4:5]
	global_load_lds_dwordx4 v163, s[40:41]
	s_add_i32 m0, s51, 0x6000
	s_nop 0
	global_load_lds_dwordx4 v162, s[40:41]
.LBB0_732:
	s_cmp_lg_u64 s[2:3], 0
	s_cbranch_scc1 .Lswp_guO_half
	ds_read_b64_tr_b16 v[162:163], v190 offset:32768
	ds_read_b64_tr_b16 v[164:165], v191 offset:32768
	ds_read_b64_tr_b16 v[166:167], v190 offset:40960
	ds_read_b64_tr_b16 v[168:169], v191 offset:40960
	ds_read_b64_tr_b16 v[170:171], v192 offset:32768
	ds_read_b64_tr_b16 v[172:173], v193 offset:32768
	ds_read_b64_tr_b16 v[174:175], v192 offset:40960
	ds_read_b64_tr_b16 v[176:177], v193 offset:40960
	ds_read_b128 v[214:217], v207 offset:32768
	ds_read_b128 v[224:227], v207 offset:34816
	ds_read_b128 v[232:235], v207 offset:36864
	ds_read_b128 v[240:243], v207 offset:38912
	ds_read_b128 v[218:221], v207 offset:33792
	ds_read_b128 v[228:231], v207 offset:35840
	ds_read_b128 v[236:239], v207 offset:37888
	ds_read_b128 v[244:247], v207 offset:39936
	s_setprio 1
	s_waitcnt lgkmcnt(7)
	v_mfma_f32_16x16x32_bf16 v[158:161], v[162:165], v[214:217], v[158:161]
	v_mfma_f32_16x16x32_bf16 v[154:157], v[170:173], v[214:217], v[154:157]
	ds_read_b128 v[214:217], v207 offset:49152
	s_waitcnt lgkmcnt(7)
	v_mfma_f32_16x16x32_bf16 v[146:149], v[162:165], v[224:227], v[146:149]
	v_mfma_f32_16x16x32_bf16 v[138:141], v[170:173], v[224:227], v[138:141]
	ds_read_b128 v[224:227], v207 offset:51200
	s_waitcnt lgkmcnt(7)
	v_mfma_f32_16x16x32_bf16 v[130:133], v[162:165], v[232:235], v[130:133]
	v_mfma_f32_16x16x32_bf16 v[122:125], v[170:173], v[232:235], v[122:125]
	ds_read_b128 v[232:235], v207 offset:53248
	s_waitcnt lgkmcnt(7)
	v_mfma_f32_16x16x32_bf16 v[114:117], v[162:165], v[240:243], v[114:117]
	v_mfma_f32_16x16x32_bf16 v[106:109], v[170:173], v[240:243], v[106:109]
	ds_read_b128 v[240:243], v207 offset:55296
	s_waitcnt lgkmcnt(7)
	v_mfma_f32_16x16x32_bf16 v[158:161], v[166:169], v[218:221], v[158:161]
	v_mfma_f32_16x16x32_bf16 v[154:157], v[174:177], v[218:221], v[154:157]
	ds_read_b128 v[218:221], v207 offset:50176
	s_waitcnt lgkmcnt(7)
	v_mfma_f32_16x16x32_bf16 v[146:149], v[166:169], v[228:231], v[146:149]
	v_mfma_f32_16x16x32_bf16 v[138:141], v[174:177], v[228:231], v[138:141]
	ds_read_b128 v[228:231], v207 offset:52224
	s_waitcnt lgkmcnt(7)
	v_mfma_f32_16x16x32_bf16 v[130:133], v[166:169], v[236:239], v[130:133]
	v_mfma_f32_16x16x32_bf16 v[122:125], v[174:177], v[236:239], v[122:125]
	ds_read_b128 v[236:239], v207 offset:54272
	s_waitcnt lgkmcnt(7)
	v_mfma_f32_16x16x32_bf16 v[114:117], v[166:169], v[244:247], v[114:117]
	v_mfma_f32_16x16x32_bf16 v[106:109], v[174:177], v[244:247], v[106:109]
	ds_read_b128 v[244:247], v207 offset:56320
	s_waitcnt lgkmcnt(7)
	v_mfma_f32_16x16x32_bf16 v[94:97], v[162:165], v[214:217], v[94:97]
	v_mfma_f32_16x16x32_bf16 v[86:89], v[170:173], v[214:217], v[86:89]
	ds_read_b128 v[214:217], v207 offset:32768
	s_waitcnt lgkmcnt(7)
	v_mfma_f32_16x16x32_bf16 v[78:81], v[162:165], v[224:227], v[78:81]
	v_mfma_f32_16x16x32_bf16 v[70:73], v[170:173], v[224:227], v[70:73]
	ds_read_b128 v[224:227], v207 offset:34816
	s_waitcnt lgkmcnt(7)
	v_mfma_f32_16x16x32_bf16 v[62:65], v[162:165], v[232:235], v[62:65]
	v_mfma_f32_16x16x32_bf16 v[54:57], v[170:173], v[232:235], v[54:57]
	ds_read_b128 v[232:235], v207 offset:36864
	s_waitcnt lgkmcnt(7)
	v_mfma_f32_16x16x32_bf16 v[46:49], v[162:165], v[240:243], v[46:49]
	v_mfma_f32_16x16x32_bf16 v[38:41], v[170:173], v[240:243], v[38:41]
	ds_read_b128 v[240:243], v207 offset:38912
	ds_read_b64_tr_b16 v[162:163], v190 offset:49152
	ds_read_b64_tr_b16 v[164:165], v191 offset:49152
	ds_read_b64_tr_b16 v[170:171], v192 offset:49152
	ds_read_b64_tr_b16 v[172:173], v193 offset:49152
	s_waitcnt lgkmcnt(11)
	v_mfma_f32_16x16x32_bf16 v[94:97], v[166:169], v[218:221], v[94:97]
	v_mfma_f32_16x16x32_bf16 v[86:89], v[174:177], v[218:221], v[86:89]
	ds_read_b128 v[218:221], v207 offset:33792
	s_waitcnt lgkmcnt(11)
	v_mfma_f32_16x16x32_bf16 v[78:81], v[166:169], v[228:231], v[78:81]
	v_mfma_f32_16x16x32_bf16 v[70:73], v[174:177], v[228:231], v[70:73]
	ds_read_b128 v[228:231], v207 offset:35840
	s_waitcnt lgkmcnt(11)
	v_mfma_f32_16x16x32_bf16 v[62:65], v[166:169], v[236:239], v[62:65]
	v_mfma_f32_16x16x32_bf16 v[54:57], v[174:177], v[236:239], v[54:57]
	ds_read_b128 v[236:239], v207 offset:37888
	s_waitcnt lgkmcnt(11)
	v_mfma_f32_16x16x32_bf16 v[46:49], v[166:169], v[244:247], v[46:49]
	v_mfma_f32_16x16x32_bf16 v[38:41], v[174:177], v[244:247], v[38:41]
	ds_read_b128 v[244:247], v207 offset:39936
	ds_read_b64_tr_b16 v[166:167], v190 offset:57344
	ds_read_b64_tr_b16 v[168:169], v191 offset:57344
	ds_read_b64_tr_b16 v[174:175], v192 offset:57344
	ds_read_b64_tr_b16 v[176:177], v193 offset:57344
	s_waitcnt lgkmcnt(8)
	v_mfma_f32_16x16x32_bf16 v[150:153], v[162:165], v[214:217], v[150:153]
	v_mfma_f32_16x16x32_bf16 v[142:145], v[170:173], v[214:217], v[142:145]
	ds_read_b128 v[214:217], v207 offset:49152
	v_mfma_f32_16x16x32_bf16 v[134:137], v[162:165], v[224:227], v[134:137]
	v_mfma_f32_16x16x32_bf16 v[126:129], v[170:173], v[224:227], v[126:129]
	ds_read_b128 v[224:227], v207 offset:51200
	v_mfma_f32_16x16x32_bf16 v[118:121], v[162:165], v[232:235], v[118:121]
	v_mfma_f32_16x16x32_bf16 v[110:113], v[170:173], v[232:235], v[110:113]
	ds_read_b128 v[232:235], v207 offset:53248
	v_mfma_f32_16x16x32_bf16 v[102:105], v[162:165], v[240:243], v[102:105]
	v_mfma_f32_16x16x32_bf16 v[98:101], v[170:173], v[240:243], v[98:101]
	ds_read_b128 v[240:243], v207 offset:55296
	s_waitcnt lgkmcnt(4)
	v_mfma_f32_16x16x32_bf16 v[150:153], v[166:169], v[218:221], v[150:153]
	v_mfma_f32_16x16x32_bf16 v[142:145], v[174:177], v[218:221], v[142:145]
	ds_read_b128 v[218:221], v207 offset:50176
	v_mfma_f32_16x16x32_bf16 v[134:137], v[166:169], v[228:231], v[134:137]
	v_mfma_f32_16x16x32_bf16 v[126:129], v[174:177], v[228:231], v[126:129]
	ds_read_b128 v[228:231], v207 offset:52224
	v_mfma_f32_16x16x32_bf16 v[118:121], v[166:169], v[236:239], v[118:121]
	v_mfma_f32_16x16x32_bf16 v[110:113], v[174:177], v[236:239], v[110:113]
	ds_read_b128 v[236:239], v207 offset:54272
	v_mfma_f32_16x16x32_bf16 v[102:105], v[166:169], v[244:247], v[102:105]
	v_mfma_f32_16x16x32_bf16 v[98:101], v[174:177], v[244:247], v[98:101]
	ds_read_b128 v[244:247], v207 offset:56320
	s_waitcnt lgkmcnt(7)
	v_mfma_f32_16x16x32_bf16 v[90:93], v[162:165], v[214:217], v[90:93]
	v_mfma_f32_16x16x32_bf16 v[82:85], v[170:173], v[214:217], v[82:85]
	s_waitcnt vmcnt(9)
	v_cvt_pk_bf16_f32 v34, v34, v35
	v_cvt_pk_bf16_f32 v35, v36, v37
	ds_write_b64 v194, v[34:35]
	s_waitcnt lgkmcnt(7)
	v_mfma_f32_16x16x32_bf16 v[74:77], v[162:165], v[224:227], v[74:77]
	v_mfma_f32_16x16x32_bf16 v[66:69], v[170:173], v[224:227], v[66:69]
	s_waitcnt vmcnt(8)
	v_cvt_pk_bf16_f32 v22, v22, v23
	v_cvt_pk_bf16_f32 v23, v24, v25
	ds_write_b64 v194, v[22:23] offset:16384
	s_waitcnt lgkmcnt(7)
	v_mfma_f32_16x16x32_bf16 v[58:61], v[162:165], v[232:235], v[58:61]
	v_mfma_f32_16x16x32_bf16 v[50:53], v[170:173], v[232:235], v[50:53]
	s_waitcnt vmcnt(7)
	v_cvt_pk_bf16_f32 v22, v26, v27
	v_cvt_pk_bf16_f32 v23, v28, v29
	ds_write_b64 v195, v[22:23]
	s_waitcnt lgkmcnt(7)
	v_mfma_f32_16x16x32_bf16 v[42:45], v[162:165], v[240:243], v[42:45]
	v_mfma_f32_16x16x32_bf16 v[30:33], v[170:173], v[240:243], v[30:33]
	s_waitcnt vmcnt(6)
	v_cvt_pk_bf16_f32 v14, v14, v15
	v_cvt_pk_bf16_f32 v15, v16, v17
	ds_write_b64 v195, v[14:15] offset:16384
	s_waitcnt lgkmcnt(7)
	v_mfma_f32_16x16x32_bf16 v[90:93], v[166:169], v[218:221], v[90:93]
	v_mfma_f32_16x16x32_bf16 v[82:85], v[174:177], v[218:221], v[82:85]
	s_waitcnt vmcnt(5)
	v_cvt_pk_bf16_f32 v14, v18, v19
	v_cvt_pk_bf16_f32 v15, v20, v21
	ds_write_b64 v196, v[14:15]
	s_waitcnt lgkmcnt(7)
	v_mfma_f32_16x16x32_bf16 v[74:77], v[166:169], v[228:231], v[74:77]
	v_mfma_f32_16x16x32_bf16 v[66:69], v[174:177], v[228:231], v[66:69]
	s_waitcnt vmcnt(4)
	v_cvt_pk_bf16_f32 v6, v6, v7
	v_cvt_pk_bf16_f32 v7, v8, v9
	ds_write_b64 v196, v[6:7] offset:16384
	s_waitcnt lgkmcnt(7)
	v_mfma_f32_16x16x32_bf16 v[58:61], v[166:169], v[236:239], v[58:61]
	v_mfma_f32_16x16x32_bf16 v[50:53], v[174:177], v[236:239], v[50:53]
	s_waitcnt vmcnt(3)
	v_cvt_pk_bf16_f32 v6, v10, v11
	v_cvt_pk_bf16_f32 v7, v12, v13
	ds_write_b64 v197, v[6:7]
	s_waitcnt lgkmcnt(7)
	v_mfma_f32_16x16x32_bf16 v[42:45], v[166:169], v[244:247], v[42:45]
	v_mfma_f32_16x16x32_bf16 v[30:33], v[174:177], v[244:247], v[30:33]
	s_waitcnt vmcnt(2)
	v_cvt_pk_bf16_f32 v2, v2, v3
	v_cvt_pk_bf16_f32 v3, v4, v5
	ds_write_b64 v197, v[2:3] offset:16384
	s_setprio 0

.Lswp_guO_tail:
	s_add_u32 s4, s35, s4
	s_addc_u32 s5, s34, s5
	s_add_u32 s34, s2, 0x2000
	s_addc_u32 s35, s3, 0
	global_load_dwordx4 v[2:5], v189, s[2:3]
	s_add_u32 s38, s4, 0x2000
	global_load_dwordx4 v[6:9], v189, s[4:5]
	s_addc_u32 s39, s5, 0
	global_load_dwordx4 v[10:13], v189, s[34:35]
	s_add_u32 s34, s2, 0x4000
	s_addc_u32 s35, s3, 0
	global_load_dwordx4 v[14:17], v189, s[38:39]
	s_add_u32 s38, s4, 0x4000
	s_addc_u32 s39, s5, 0
	global_load_dwordx4 v[18:21], v189, s[34:35]
	s_add_u32 s2, s2, 0x6000
	global_load_dwordx4 v[22:25], v189, s[38:39]
	s_addc_u32 s3, s3, 0
	s_add_u32 s4, s4, 0x6000
	global_load_dwordx4 v[26:29], v189, s[2:3]
	s_addc_u32 s5, s5, 0
	global_load_dwordx4 v[34:37], v189, s[4:5]
	s_waitcnt vmcnt(8)
	s_waitcnt lgkmcnt(0)
	s_barrier
	s_cmp_gt_u32 s17, 29
	s_cbranch_scc1 .LBB0_738
	s_mov_b32 s34, s17
	s_branch .LBB0_724

.Lswqd_guE:
	v_cvt_pk_bf16_f32 v2, v2, v3
	v_cvt_pk_bf16_f32 v3, v4, v5
	ds_write_b64 v199, v[2:3]
	v_cvt_pk_bf16_f32 v2, v6, v7
	v_cvt_pk_bf16_f32 v3, v8, v9
	ds_write_b64 v200, v[2:3]
	v_cvt_pk_bf16_f32 v2, v10, v11
	v_cvt_pk_bf16_f32 v3, v12, v13
	ds_write_b64 v201, v[2:3]
	v_cvt_pk_bf16_f32 v2, v14, v15
	v_cvt_pk_bf16_f32 v3, v16, v17
	ds_write_b64 v202, v[2:3]
	v_cvt_pk_bf16_f32 v2, v18, v19
	v_cvt_pk_bf16_f32 v3, v20, v21
	ds_write_b64 v203, v[2:3]
	v_cvt_pk_bf16_f32 v2, v22, v23
	v_cvt_pk_bf16_f32 v3, v24, v25
	ds_write_b64 v204, v[2:3]
	v_cvt_pk_bf16_f32 v2, v26, v27
	v_cvt_pk_bf16_f32 v3, v28, v29
	ds_write_b64 v205, v[2:3]
	v_cvt_pk_bf16_f32 v2, v34, v35
	v_cvt_pk_bf16_f32 v3, v36, v37
	ds_write_b64 v206, v[2:3]
	s_branch .Lswp_guE_tail

.Lswqd_guO:
	v_cvt_pk_bf16_f32 v34, v34, v35
	v_cvt_pk_bf16_f32 v35, v36, v37
	ds_write_b64 v194, v[34:35]
	v_cvt_pk_bf16_f32 v22, v22, v23
	v_cvt_pk_bf16_f32 v23, v24, v25
	ds_write_b64 v194, v[22:23] offset:16384
	v_cvt_pk_bf16_f32 v22, v26, v27
	v_cvt_pk_bf16_f32 v23, v28, v29
	ds_write_b64 v195, v[22:23]
	v_cvt_pk_bf16_f32 v14, v14, v15
	v_cvt_pk_bf16_f32 v15, v16, v17
	ds_write_b64 v195, v[14:15] offset:16384
	v_cvt_pk_bf16_f32 v14, v18, v19
	v_cvt_pk_bf16_f32 v15, v20, v21
	ds_write_b64 v196, v[14:15]
	v_cvt_pk_bf16_f32 v6, v6, v7
	v_cvt_pk_bf16_f32 v7, v8, v9
	ds_write_b64 v196, v[6:7] offset:16384
	v_cvt_pk_bf16_f32 v6, v10, v11
	v_cvt_pk_bf16_f32 v7, v12, v13
	ds_write_b64 v197, v[6:7]
	v_cvt_pk_bf16_f32 v2, v2, v3
	v_cvt_pk_bf16_f32 v3, v4, v5
	ds_write_b64 v197, v[2:3] offset:16384
	s_branch .Lswp_guO_tail

.LBB0_858:
	s_cmp_lg_u64 s[2:3], 0
	s_cbranch_scc1 .Lswp_dnE_half
	ds_read_b64_tr_b16 v[164:165], v190 offset:0
	ds_read_b64_tr_b16 v[166:167], v191 offset:0
	ds_read_b64_tr_b16 v[168:169], v190 offset:8192
	ds_read_b64_tr_b16 v[170:171], v191 offset:8192
	ds_read_b64_tr_b16 v[172:173], v192 offset:0
	ds_read_b64_tr_b16 v[174:175], v193 offset:0
	ds_read_b64_tr_b16 v[176:177], v192 offset:8192
	ds_read_b64_tr_b16 v[178:179], v193 offset:8192
	ds_read_b128 v[210:213], v207
	ds_read_b128 v[218:221], v207 offset:2048
	ds_read_b128 v[228:231], v207 offset:4096
	ds_read_b128 v[236:239], v207 offset:6144
	ds_read_b128 v[214:217], v207 offset:1024
	ds_read_b128 v[224:227], v207 offset:3072
	ds_read_b128 v[232:235], v207 offset:5120
	ds_read_b128 v[240:243], v207 offset:7168
	s_setprio 1
	s_waitcnt lgkmcnt(7)
	v_mfma_f32_16x16x32_bf16 v[160:163], v[164:167], v[210:213], v[160:163]
	v_mfma_f32_16x16x32_bf16 v[156:159], v[172:175], v[210:213], v[156:159]
	ds_read_b128 v[210:213], v207 offset:16384
	s_waitcnt lgkmcnt(7)
	v_mfma_f32_16x16x32_bf16 v[152:155], v[164:167], v[218:221], v[152:155]
	v_mfma_f32_16x16x32_bf16 v[148:151], v[172:175], v[218:221], v[148:151]
	ds_read_b128 v[218:221], v207 offset:18432
	s_waitcnt lgkmcnt(7)
	v_mfma_f32_16x16x32_bf16 v[136:139], v[164:167], v[228:231], v[136:139]
	v_mfma_f32_16x16x32_bf16 v[132:135], v[172:175], v[228:231], v[132:135]
	ds_read_b128 v[228:231], v207 offset:20480
	s_waitcnt lgkmcnt(7)
	v_mfma_f32_16x16x32_bf16 v[120:123], v[164:167], v[236:239], v[120:123]
	v_mfma_f32_16x16x32_bf16 v[116:119], v[172:175], v[236:239], v[116:119]
	ds_read_b128 v[236:239], v207 offset:22528
	s_waitcnt lgkmcnt(7)
	v_mfma_f32_16x16x32_bf16 v[160:163], v[168:171], v[214:217], v[160:163]
	v_mfma_f32_16x16x32_bf16 v[156:159], v[176:179], v[214:217], v[156:159]
	ds_read_b128 v[214:217], v207 offset:17408
	s_waitcnt lgkmcnt(7)
	v_mfma_f32_16x16x32_bf16 v[152:155], v[168:171], v[224:227], v[152:155]
	v_mfma_f32_16x16x32_bf16 v[148:151], v[176:179], v[224:227], v[148:151]
	ds_read_b128 v[224:227], v207 offset:19456
	s_waitcnt lgkmcnt(7)
	v_mfma_f32_16x16x32_bf16 v[136:139], v[168:171], v[232:235], v[136:139]
	v_mfma_f32_16x16x32_bf16 v[132:135], v[176:179], v[232:235], v[132:135]
	ds_read_b128 v[232:235], v207 offset:21504
	s_waitcnt lgkmcnt(7)
	v_mfma_f32_16x16x32_bf16 v[120:123], v[168:171], v[240:243], v[120:123]
	v_mfma_f32_16x16x32_bf16 v[116:119], v[176:179], v[240:243], v[116:119]
	ds_read_b128 v[240:243], v207 offset:23552
	s_waitcnt lgkmcnt(7)
	v_mfma_f32_16x16x32_bf16 v[80:83], v[164:167], v[210:213], v[80:83]
	v_mfma_f32_16x16x32_bf16 v[68:71], v[172:175], v[210:213], v[68:71]
	ds_read_b128 v[210:213], v207
	s_waitcnt lgkmcnt(7)
	v_mfma_f32_16x16x32_bf16 v[48:51], v[164:167], v[218:221], v[48:51]
	v_mfma_f32_16x16x32_bf16 v[44:47], v[172:175], v[218:221], v[44:47]
	ds_read_b128 v[218:221], v207 offset:2048
	s_waitcnt lgkmcnt(7)
	v_mfma_f32_16x16x32_bf16 v[32:35], v[164:167], v[228:231], v[32:35]
	v_mfma_f32_16x16x32_bf16 v[28:31], v[172:175], v[228:231], v[28:31]
	ds_read_b128 v[228:231], v207 offset:4096
	s_waitcnt lgkmcnt(7)
	v_mfma_f32_16x16x32_bf16 v[16:19], v[164:167], v[236:239], v[16:19]
	v_mfma_f32_16x16x32_bf16 v[12:15], v[172:175], v[236:239], v[12:15]
	ds_read_b128 v[236:239], v207 offset:6144
	ds_read_b64_tr_b16 v[164:165], v190 offset:16384
	ds_read_b64_tr_b16 v[166:167], v191 offset:16384
	ds_read_b64_tr_b16 v[172:173], v192 offset:16384
	ds_read_b64_tr_b16 v[174:175], v193 offset:16384
	s_waitcnt lgkmcnt(11)
	v_mfma_f32_16x16x32_bf16 v[80:83], v[168:171], v[214:217], v[80:83]
	v_mfma_f32_16x16x32_bf16 v[68:71], v[176:179], v[214:217], v[68:71]
	ds_read_b128 v[214:217], v207 offset:1024
	s_waitcnt lgkmcnt(11)
	v_mfma_f32_16x16x32_bf16 v[48:51], v[168:171], v[224:227], v[48:51]
	v_mfma_f32_16x16x32_bf16 v[44:47], v[176:179], v[224:227], v[44:47]
	ds_read_b128 v[224:227], v207 offset:3072
	s_waitcnt lgkmcnt(11)
	v_mfma_f32_16x16x32_bf16 v[32:35], v[168:171], v[232:235], v[32:35]
	v_mfma_f32_16x16x32_bf16 v[28:31], v[176:179], v[232:235], v[28:31]
	ds_read_b128 v[232:235], v207 offset:5120
	s_waitcnt lgkmcnt(11)
	v_mfma_f32_16x16x32_bf16 v[16:19], v[168:171], v[240:243], v[16:19]
	v_mfma_f32_16x16x32_bf16 v[12:15], v[176:179], v[240:243], v[12:15]
	ds_read_b128 v[240:243], v207 offset:7168
	ds_read_b64_tr_b16 v[168:169], v190 offset:24576
	ds_read_b64_tr_b16 v[170:171], v191 offset:24576
	ds_read_b64_tr_b16 v[176:177], v192 offset:24576
	ds_read_b64_tr_b16 v[178:179], v193 offset:24576
	s_waitcnt lgkmcnt(8)
	v_mfma_f32_16x16x32_bf16 v[144:147], v[164:167], v[210:213], v[144:147]
	v_mfma_f32_16x16x32_bf16 v[140:143], v[172:175], v[210:213], v[140:143]
	ds_read_b128 v[210:213], v207 offset:16384
	v_mfma_f32_16x16x32_bf16 v[128:131], v[164:167], v[218:221], v[128:131]
	v_mfma_f32_16x16x32_bf16 v[124:127], v[172:175], v[218:221], v[124:127]
	ds_read_b128 v[218:221], v207 offset:18432
	v_mfma_f32_16x16x32_bf16 v[112:115], v[164:167], v[228:231], v[112:115]
	v_mfma_f32_16x16x32_bf16 v[108:111], v[172:175], v[228:231], v[108:111]
	ds_read_b128 v[228:231], v207 offset:20480
	v_mfma_f32_16x16x32_bf16 v[104:107], v[164:167], v[236:239], v[104:107]
	v_mfma_f32_16x16x32_bf16 v[100:103], v[172:175], v[236:239], v[100:103]
	ds_read_b128 v[236:239], v207 offset:22528
	s_waitcnt lgkmcnt(4)
	v_mfma_f32_16x16x32_bf16 v[144:147], v[168:171], v[214:217], v[144:147]
	v_mfma_f32_16x16x32_bf16 v[140:143], v[176:179], v[214:217], v[140:143]
	ds_read_b128 v[214:217], v207 offset:17408
	v_mfma_f32_16x16x32_bf16 v[128:131], v[168:171], v[224:227], v[128:131]
	v_mfma_f32_16x16x32_bf16 v[124:127], v[176:179], v[224:227], v[124:127]
	ds_read_b128 v[224:227], v207 offset:19456
	v_mfma_f32_16x16x32_bf16 v[112:115], v[168:171], v[232:235], v[112:115]
	v_mfma_f32_16x16x32_bf16 v[108:111], v[176:179], v[232:235], v[108:111]
	ds_read_b128 v[232:235], v207 offset:21504
	v_mfma_f32_16x16x32_bf16 v[104:107], v[168:171], v[240:243], v[104:107]
	v_mfma_f32_16x16x32_bf16 v[100:103], v[176:179], v[240:243], v[100:103]
	ds_read_b128 v[240:243], v207 offset:23552
	s_waitcnt lgkmcnt(7)
	v_mfma_f32_16x16x32_bf16 v[56:59], v[164:167], v[210:213], v[56:59]
	v_mfma_f32_16x16x32_bf16 v[52:55], v[172:175], v[210:213], v[52:55]
	s_waitcnt vmcnt(11)
	v_cvt_pk_bf16_f32 v244, v64, v65
	v_cvt_pk_bf16_f32 v245, v66, v67
	ds_write_b64 v199, v[244:245]
	s_waitcnt lgkmcnt(7)
	v_mfma_f32_16x16x32_bf16 v[40:43], v[164:167], v[218:221], v[40:43]
	v_mfma_f32_16x16x32_bf16 v[36:39], v[172:175], v[218:221], v[36:39]
	s_waitcnt vmcnt(10)
	v_cvt_pk_bf16_f32 v244, v60, v61
	v_cvt_pk_bf16_f32 v245, v62, v63
	ds_write_b64 v200, v[244:245]
	s_waitcnt lgkmcnt(7)
	v_mfma_f32_16x16x32_bf16 v[24:27], v[164:167], v[228:231], v[24:27]
	v_mfma_f32_16x16x32_bf16 v[20:23], v[172:175], v[228:231], v[20:23]
	s_waitcnt vmcnt(9)
	v_cvt_pk_bf16_f32 v244, v76, v77
	v_cvt_pk_bf16_f32 v245, v78, v79
	ds_write_b64 v201, v[244:245]
	s_waitcnt lgkmcnt(7)
	v_mfma_f32_16x16x32_bf16 v[8:11], v[164:167], v[236:239], v[8:11]
	v_mfma_f32_16x16x32_bf16 v[2:5], v[172:175], v[236:239], v[4:7]
	s_waitcnt vmcnt(8)
	v_cvt_pk_bf16_f32 v244, v72, v73
	v_cvt_pk_bf16_f32 v245, v74, v75
	ds_write_b64 v202, v[244:245]
	s_waitcnt lgkmcnt(7)
	v_mfma_f32_16x16x32_bf16 v[56:59], v[168:171], v[214:217], v[56:59]
	v_mfma_f32_16x16x32_bf16 v[52:55], v[176:179], v[214:217], v[52:55]
	s_waitcnt vmcnt(7)
	v_cvt_pk_bf16_f32 v244, v88, v89
	v_cvt_pk_bf16_f32 v245, v90, v91
	ds_write_b64 v203, v[244:245]
	s_waitcnt lgkmcnt(7)
	v_mfma_f32_16x16x32_bf16 v[40:43], v[168:171], v[224:227], v[40:43]
	v_mfma_f32_16x16x32_bf16 v[36:39], v[176:179], v[224:227], v[36:39]
	s_waitcnt vmcnt(6)
	v_cvt_pk_bf16_f32 v244, v84, v85
	v_cvt_pk_bf16_f32 v245, v86, v87
	ds_write_b64 v204, v[244:245]
	s_waitcnt lgkmcnt(7)
	v_mfma_f32_16x16x32_bf16 v[24:27], v[168:171], v[232:235], v[24:27]
	v_mfma_f32_16x16x32_bf16 v[20:23], v[176:179], v[232:235], v[20:23]
	s_waitcnt vmcnt(5)
	v_cvt_pk_bf16_f32 v244, v96, v97
	v_cvt_pk_bf16_f32 v245, v98, v99
	ds_write_b64 v205, v[244:245]
	s_waitcnt lgkmcnt(7)
	v_mfma_f32_16x16x32_bf16 v[8:11], v[168:171], v[240:243], v[8:11]
	v_mfma_f32_16x16x32_bf16 v[4:7], v[176:179], v[240:243], v[2:5]
	s_waitcnt vmcnt(4)
	v_cvt_pk_bf16_f32 v244, v92, v93
	v_cvt_pk_bf16_f32 v245, v94, v95
	ds_write_b64 v206, v[244:245]
	s_setprio 0

.Lswp_dnE_tail:
	s_ashr_i32 s49, s48, 31
	s_lshl_b64 s[50:51], s[48:49], 19
	s_add_u32 s72, s74, s50
	s_addc_u32 s73, s43, s51
	s_add_u32 s50, s37, s50
	s_addc_u32 s51, s35, s51
	s_add_u32 s78, s72, 0x4000
	s_addc_u32 s79, s73, 0
	global_load_dwordx4 v[96:99], v189, s[72:73]
	s_add_u32 s80, s50, 0x4000
	global_load_dwordx4 v[88:91], v189, s[50:51]
	s_addc_u32 s81, s51, 0
	global_load_dwordx4 v[92:95], v189, s[78:79]
	s_add_u32 s78, s72, 0x8000
	s_addc_u32 s79, s73, 0
	global_load_dwordx4 v[76:79], v189, s[80:81]
	s_add_u32 s80, s50, 0x8000
	s_addc_u32 s81, s51, 0
	s_add_u32 s72, s72, 0xc000
	global_load_dwordx4 v[84:87], v189, s[78:79]
	s_addc_u32 s73, s73, 0
	global_load_dwordx4 v[64:67], v189, s[80:81]
	s_add_u32 s50, s50, 0xc000
	s_addc_u32 s51, s51, 0
	global_load_dwordx4 v[72:75], v189, s[72:73]
	global_load_dwordx4 v[60:63], v189, s[50:51]
	s_lshl_b64 s[50:51], s[48:49], 7
	s_add_u32 s50, s82, s50
	s_addc_u32 s51, s77, s51
	s_mov_b32 m0, s21
	s_waitcnt vmcnt(8)
	s_waitcnt lgkmcnt(0)
	s_barrier
	v_lshl_add_u64 v[2:3], s[50:51], 0, v[180:181]
	global_load_lds_dwordx4 v[2:3], off
	v_lshl_add_u64 v[2:3], s[50:51], 0, v[182:183]
	s_mov_b32 m0, s67
	v_cndmask_b32_e32 v1, v209, v208, vcc
	global_load_lds_dwordx4 v[2:3], off
	v_cmp_ne_u32_e32 vcc, 0, v1
	s_mov_b64 s[96:97], vcc
	s_cbranch_vccnz .LBB0_864
	v_lshl_add_u64 v[164:165], s[50:51], 0, v[184:185]
	s_add_i32 m0, s21, 0x4000
	v_lshl_add_u64 v[2:3], s[50:51], 0, v[186:187]
	global_load_lds_dwordx4 v[164:165], off
	s_add_i32 m0, s21, 0x6000
	s_nop 0
	global_load_lds_dwordx4 v[2:3], off
.LBB0_864:
	s_cmp_lg_u64 s[2:3], 0
	s_cbranch_scc1 .Lswp_dnO_half
	ds_read_b64_tr_b16 v[164:165], v190 offset:32768
	ds_read_b64_tr_b16 v[166:167], v191 offset:32768
	ds_read_b64_tr_b16 v[168:169], v190 offset:40960
	ds_read_b64_tr_b16 v[170:171], v191 offset:40960
	ds_read_b64_tr_b16 v[172:173], v192 offset:32768
	ds_read_b64_tr_b16 v[174:175], v193 offset:32768
	ds_read_b64_tr_b16 v[176:177], v192 offset:40960
	ds_read_b64_tr_b16 v[178:179], v193 offset:40960
	ds_read_b128 v[210:213], v207 offset:32768
	ds_read_b128 v[218:221], v207 offset:34816
	ds_read_b128 v[228:231], v207 offset:36864
	ds_read_b128 v[236:239], v207 offset:38912
	ds_read_b128 v[214:217], v207 offset:33792
	ds_read_b128 v[224:227], v207 offset:35840
	ds_read_b128 v[232:235], v207 offset:37888
	ds_read_b128 v[240:243], v207 offset:39936
	s_setprio 1
	s_waitcnt lgkmcnt(7)
	v_mfma_f32_16x16x32_bf16 v[160:163], v[164:167], v[210:213], v[160:163]
	v_mfma_f32_16x16x32_bf16 v[156:159], v[172:175], v[210:213], v[156:159]
	ds_read_b128 v[210:213], v207 offset:49152
	s_waitcnt lgkmcnt(7)
	v_mfma_f32_16x16x32_bf16 v[152:155], v[164:167], v[218:221], v[152:155]
	v_mfma_f32_16x16x32_bf16 v[148:151], v[172:175], v[218:221], v[148:151]
	ds_read_b128 v[218:221], v207 offset:51200
	s_waitcnt lgkmcnt(7)
	v_mfma_f32_16x16x32_bf16 v[136:139], v[164:167], v[228:231], v[136:139]
	v_mfma_f32_16x16x32_bf16 v[132:135], v[172:175], v[228:231], v[132:135]
	ds_read_b128 v[228:231], v207 offset:53248
	s_waitcnt lgkmcnt(7)
	v_mfma_f32_16x16x32_bf16 v[120:123], v[164:167], v[236:239], v[120:123]
	v_mfma_f32_16x16x32_bf16 v[116:119], v[172:175], v[236:239], v[116:119]
	ds_read_b128 v[236:239], v207 offset:55296
	s_waitcnt lgkmcnt(7)
	v_mfma_f32_16x16x32_bf16 v[160:163], v[168:171], v[214:217], v[160:163]
	v_mfma_f32_16x16x32_bf16 v[156:159], v[176:179], v[214:217], v[156:159]
	ds_read_b128 v[214:217], v207 offset:50176
	s_waitcnt lgkmcnt(7)
	v_mfma_f32_16x16x32_bf16 v[152:155], v[168:171], v[224:227], v[152:155]
	v_mfma_f32_16x16x32_bf16 v[148:151], v[176:179], v[224:227], v[148:151]
	ds_read_b128 v[224:227], v207 offset:52224
	s_waitcnt lgkmcnt(7)
	v_mfma_f32_16x16x32_bf16 v[136:139], v[168:171], v[232:235], v[136:139]
	v_mfma_f32_16x16x32_bf16 v[132:135], v[176:179], v[232:235], v[132:135]
	ds_read_b128 v[232:235], v207 offset:54272
	s_waitcnt lgkmcnt(7)
	v_mfma_f32_16x16x32_bf16 v[120:123], v[168:171], v[240:243], v[120:123]
	v_mfma_f32_16x16x32_bf16 v[116:119], v[176:179], v[240:243], v[116:119]
	ds_read_b128 v[240:243], v207 offset:56320
	s_waitcnt lgkmcnt(7)
	v_mfma_f32_16x16x32_bf16 v[80:83], v[164:167], v[210:213], v[80:83]
	v_mfma_f32_16x16x32_bf16 v[68:71], v[172:175], v[210:213], v[68:71]
	ds_read_b128 v[210:213], v207 offset:32768
	s_waitcnt lgkmcnt(7)
	v_mfma_f32_16x16x32_bf16 v[48:51], v[164:167], v[218:221], v[48:51]
	v_mfma_f32_16x16x32_bf16 v[44:47], v[172:175], v[218:221], v[44:47]
	ds_read_b128 v[218:221], v207 offset:34816
	s_waitcnt lgkmcnt(7)
	v_mfma_f32_16x16x32_bf16 v[32:35], v[164:167], v[228:231], v[32:35]
	v_mfma_f32_16x16x32_bf16 v[28:31], v[172:175], v[228:231], v[28:31]
	ds_read_b128 v[228:231], v207 offset:36864
	s_waitcnt lgkmcnt(7)
	v_mfma_f32_16x16x32_bf16 v[16:19], v[164:167], v[236:239], v[16:19]
	v_mfma_f32_16x16x32_bf16 v[12:15], v[172:175], v[236:239], v[12:15]
	ds_read_b128 v[236:239], v207 offset:38912
	ds_read_b64_tr_b16 v[164:165], v190 offset:49152
	ds_read_b64_tr_b16 v[166:167], v191 offset:49152
	ds_read_b64_tr_b16 v[172:173], v192 offset:49152
	ds_read_b64_tr_b16 v[174:175], v193 offset:49152
	s_waitcnt lgkmcnt(11)
	v_mfma_f32_16x16x32_bf16 v[80:83], v[168:171], v[214:217], v[80:83]
	v_mfma_f32_16x16x32_bf16 v[68:71], v[176:179], v[214:217], v[68:71]
	ds_read_b128 v[214:217], v207 offset:33792
	s_waitcnt lgkmcnt(11)
	v_mfma_f32_16x16x32_bf16 v[48:51], v[168:171], v[224:227], v[48:51]
	v_mfma_f32_16x16x32_bf16 v[44:47], v[176:179], v[224:227], v[44:47]
	ds_read_b128 v[224:227], v207 offset:35840
	s_waitcnt lgkmcnt(11)
	v_mfma_f32_16x16x32_bf16 v[32:35], v[168:171], v[232:235], v[32:35]
	v_mfma_f32_16x16x32_bf16 v[28:31], v[176:179], v[232:235], v[28:31]
	ds_read_b128 v[232:235], v207 offset:37888
	s_waitcnt lgkmcnt(11)
	v_mfma_f32_16x16x32_bf16 v[16:19], v[168:171], v[240:243], v[16:19]
	v_mfma_f32_16x16x32_bf16 v[12:15], v[176:179], v[240:243], v[12:15]
	ds_read_b128 v[240:243], v207 offset:39936
	ds_read_b64_tr_b16 v[168:169], v190 offset:57344
	ds_read_b64_tr_b16 v[170:171], v191 offset:57344
	ds_read_b64_tr_b16 v[176:177], v192 offset:57344
	ds_read_b64_tr_b16 v[178:179], v193 offset:57344
	s_waitcnt lgkmcnt(8)
	v_mfma_f32_16x16x32_bf16 v[144:147], v[164:167], v[210:213], v[144:147]
	v_mfma_f32_16x16x32_bf16 v[140:143], v[172:175], v[210:213], v[140:143]
	ds_read_b128 v[210:213], v207 offset:49152
	v_mfma_f32_16x16x32_bf16 v[128:131], v[164:167], v[218:221], v[128:131]
	v_mfma_f32_16x16x32_bf16 v[124:127], v[172:175], v[218:221], v[124:127]
	ds_read_b128 v[218:221], v207 offset:51200
	v_mfma_f32_16x16x32_bf16 v[112:115], v[164:167], v[228:231], v[112:115]
	v_mfma_f32_16x16x32_bf16 v[108:111], v[172:175], v[228:231], v[108:111]
	ds_read_b128 v[228:231], v207 offset:53248
	v_mfma_f32_16x16x32_bf16 v[104:107], v[164:167], v[236:239], v[104:107]
	v_mfma_f32_16x16x32_bf16 v[100:103], v[172:175], v[236:239], v[100:103]
	ds_read_b128 v[236:239], v207 offset:55296
	s_waitcnt lgkmcnt(4)
	v_mfma_f32_16x16x32_bf16 v[144:147], v[168:171], v[214:217], v[144:147]
	v_mfma_f32_16x16x32_bf16 v[140:143], v[176:179], v[214:217], v[140:143]
	ds_read_b128 v[214:217], v207 offset:50176
	v_mfma_f32_16x16x32_bf16 v[128:131], v[168:171], v[224:227], v[128:131]
	v_mfma_f32_16x16x32_bf16 v[124:127], v[176:179], v[224:227], v[124:127]
	ds_read_b128 v[224:227], v207 offset:52224
	v_mfma_f32_16x16x32_bf16 v[112:115], v[168:171], v[232:235], v[112:115]
	v_mfma_f32_16x16x32_bf16 v[108:111], v[176:179], v[232:235], v[108:111]
	ds_read_b128 v[232:235], v207 offset:54272
	v_mfma_f32_16x16x32_bf16 v[104:107], v[168:171], v[240:243], v[104:107]
	v_mfma_f32_16x16x32_bf16 v[100:103], v[176:179], v[240:243], v[100:103]
	ds_read_b128 v[240:243], v207 offset:56320
	s_waitcnt lgkmcnt(7)
	v_mfma_f32_16x16x32_bf16 v[56:59], v[164:167], v[210:213], v[56:59]
	v_mfma_f32_16x16x32_bf16 v[52:55], v[172:175], v[210:213], v[52:55]
	s_waitcnt vmcnt(9)
	v_cvt_pk_bf16_f32 v244, v96, v97
	v_cvt_pk_bf16_f32 v245, v98, v99
	ds_write_b64 v194, v[244:245]
	s_waitcnt lgkmcnt(7)
	v_mfma_f32_16x16x32_bf16 v[40:43], v[164:167], v[218:221], v[40:43]
	v_mfma_f32_16x16x32_bf16 v[36:39], v[172:175], v[218:221], v[36:39]
	s_waitcnt vmcnt(8)
	v_cvt_pk_bf16_f32 v244, v88, v89
	v_cvt_pk_bf16_f32 v245, v90, v91
	ds_write_b64 v194, v[244:245] offset:16384
	s_waitcnt lgkmcnt(7)
	v_mfma_f32_16x16x32_bf16 v[24:27], v[164:167], v[228:231], v[24:27]
	v_mfma_f32_16x16x32_bf16 v[20:23], v[172:175], v[228:231], v[20:23]
	s_waitcnt vmcnt(7)
	v_cvt_pk_bf16_f32 v244, v92, v93
	v_cvt_pk_bf16_f32 v245, v94, v95
	ds_write_b64 v195, v[244:245]
	s_waitcnt lgkmcnt(7)
	v_mfma_f32_16x16x32_bf16 v[8:11], v[164:167], v[236:239], v[8:11]
	v_mfma_f32_16x16x32_bf16 v[2:5], v[172:175], v[236:239], v[4:7]
	s_waitcnt vmcnt(6)
	v_cvt_pk_bf16_f32 v244, v76, v77
	v_cvt_pk_bf16_f32 v245, v78, v79
	ds_write_b64 v195, v[244:245] offset:16384
	s_waitcnt lgkmcnt(7)
	v_mfma_f32_16x16x32_bf16 v[56:59], v[168:171], v[214:217], v[56:59]
	v_mfma_f32_16x16x32_bf16 v[52:55], v[176:179], v[214:217], v[52:55]
	s_waitcnt vmcnt(5)
	v_cvt_pk_bf16_f32 v244, v84, v85
	v_cvt_pk_bf16_f32 v245, v86, v87
	ds_write_b64 v196, v[244:245]
	s_waitcnt lgkmcnt(7)
	v_mfma_f32_16x16x32_bf16 v[40:43], v[168:171], v[224:227], v[40:43]
	v_mfma_f32_16x16x32_bf16 v[36:39], v[176:179], v[224:227], v[36:39]
	s_waitcnt vmcnt(4)
	v_cvt_pk_bf16_f32 v244, v64, v65
	v_cvt_pk_bf16_f32 v245, v66, v67
	ds_write_b64 v196, v[244:245] offset:16384
	s_waitcnt lgkmcnt(7)
	v_mfma_f32_16x16x32_bf16 v[24:27], v[168:171], v[232:235], v[24:27]
	v_mfma_f32_16x16x32_bf16 v[20:23], v[176:179], v[232:235], v[20:23]
	s_waitcnt vmcnt(3)
	v_cvt_pk_bf16_f32 v244, v72, v73
	v_cvt_pk_bf16_f32 v245, v74, v75
	ds_write_b64 v197, v[244:245]
	s_waitcnt lgkmcnt(7)
	v_mfma_f32_16x16x32_bf16 v[8:11], v[168:171], v[240:243], v[8:11]
	v_mfma_f32_16x16x32_bf16 v[4:7], v[176:179], v[240:243], v[2:5]
	s_waitcnt vmcnt(2)
	v_cvt_pk_bf16_f32 v244, v60, v61
	v_cvt_pk_bf16_f32 v245, v62, v63
	ds_write_b64 v197, v[244:245] offset:16384
	s_setprio 0

.Lswp_dnO_tail:
	s_add_u32 s48, s2, 0x80000
	s_addc_u32 s49, s3, 0
	s_add_u32 s2, s74, s48
	s_addc_u32 s3, s43, s49
	s_add_u32 s48, s37, s48
	s_addc_u32 s49, s35, s49
	s_add_u32 s50, s2, 0x4000
	s_addc_u32 s51, s3, 0
	global_load_dwordx4 v[64:67], v189, s[2:3]
	s_add_u32 s72, s48, 0x4000
	global_load_dwordx4 v[60:63], v189, s[48:49]
	s_addc_u32 s73, s49, 0
	global_load_dwordx4 v[76:79], v189, s[50:51]
	s_add_u32 s50, s2, 0x8000
	s_addc_u32 s51, s3, 0
	global_load_dwordx4 v[72:75], v189, s[72:73]
	s_add_u32 s72, s48, 0x8000
	s_addc_u32 s73, s49, 0
	global_load_dwordx4 v[88:91], v189, s[50:51]
	s_add_u32 s2, s2, 0xc000
	global_load_dwordx4 v[84:87], v189, s[72:73]
	s_addc_u32 s3, s3, 0
	s_add_u32 s48, s48, 0xc000
	global_load_dwordx4 v[96:99], v189, s[2:3]
	s_addc_u32 s49, s49, 0
	global_load_dwordx4 v[92:95], v189, s[48:49]
	s_waitcnt vmcnt(8)
	s_waitcnt lgkmcnt(0)
	s_barrier
	s_cmp_gt_u32 s34, 13
	s_cbranch_scc1 .LBB0_870
	s_mov_b32 s35, s34
	s_branch .LBB0_856

.Lswqd_dnE:
	v_cvt_pk_bf16_f32 v2, v64, v65
	v_cvt_pk_bf16_f32 v3, v66, v67
	ds_write_b64 v199, v[2:3]
	v_cvt_pk_bf16_f32 v2, v60, v61
	v_cvt_pk_bf16_f32 v3, v62, v63
	ds_write_b64 v200, v[2:3]
	v_cvt_pk_bf16_f32 v2, v76, v77
	v_cvt_pk_bf16_f32 v3, v78, v79
	ds_write_b64 v201, v[2:3]
	v_cvt_pk_bf16_f32 v2, v72, v73
	v_cvt_pk_bf16_f32 v3, v74, v75
	ds_write_b64 v202, v[2:3]
	v_cvt_pk_bf16_f32 v2, v88, v89
	v_cvt_pk_bf16_f32 v3, v90, v91
	ds_write_b64 v203, v[2:3]
	v_cvt_pk_bf16_f32 v2, v84, v85
	v_cvt_pk_bf16_f32 v3, v86, v87
	ds_write_b64 v204, v[2:3]
	v_cvt_pk_bf16_f32 v2, v96, v97
	v_cvt_pk_bf16_f32 v3, v98, v99
	ds_write_b64 v205, v[2:3]
	v_cvt_pk_bf16_f32 v2, v92, v93
	v_cvt_pk_bf16_f32 v3, v94, v95
	ds_write_b64 v206, v[2:3]
	s_branch .Lswp_dnE_tail

.Lswqd_dnO:
	v_cvt_pk_bf16_f32 v2, v96, v97
	v_cvt_pk_bf16_f32 v3, v98, v99
	ds_write_b64 v194, v[2:3]
	v_cvt_pk_bf16_f32 v2, v88, v89
	v_cvt_pk_bf16_f32 v3, v90, v91
	ds_write_b64 v194, v[2:3] offset:16384
	v_cvt_pk_bf16_f32 v2, v92, v93
	v_cvt_pk_bf16_f32 v3, v94, v95
	ds_write_b64 v195, v[2:3]
	v_cvt_pk_bf16_f32 v2, v76, v77
	v_cvt_pk_bf16_f32 v3, v78, v79
	ds_write_b64 v195, v[2:3] offset:16384
	v_cvt_pk_bf16_f32 v2, v84, v85
	v_cvt_pk_bf16_f32 v3, v86, v87
	ds_write_b64 v196, v[2:3]
	v_cvt_pk_bf16_f32 v2, v64, v65
	v_cvt_pk_bf16_f32 v3, v66, v67
	ds_write_b64 v196, v[2:3] offset:16384
	v_cvt_pk_bf16_f32 v2, v72, v73
	v_cvt_pk_bf16_f32 v3, v74, v75
	ds_write_b64 v197, v[2:3]
	v_cvt_pk_bf16_f32 v2, v60, v61
	v_cvt_pk_bf16_f32 v3, v62, v63
	ds_write_b64 v197, v[2:3] offset:16384
	s_branch .Lswp_dnO_tail
